# v26
# speedup vs baseline: 1.0017x; 1.0017x over previous
.LBB1_3:
	s_waitcnt lgkmcnt(0)
	s_cmp_lg_u32 s31, 0
	s_cbranch_scc1 .Lk1_noprio
	s_setprio 1

.LBB2_7:
	s_cmp_lg_u32 s16, 0
	s_cbranch_scc1 .Lk2_noprio
	s_setprio 1
